# P6-hosted w_down conversion plus P4 body split in attention-only and conversion-only passes, even workgroups attention first and odd workgroups conversion first
# speedup vs baseline: 1.0071x; 1.0071x over previous
; #define LAS __attribute__((address_space(3)))
; #define LAS __attribute__((address_space(3)))
;     LAS unsigned* scr = (LAS unsigned*)(lds + wave * 16384);
;     WItem d0, d1; WRegs R0, R1;
;     constexpr int KB_ = DM / 32;
;     constexpr int NALL = EARLY ? KB_ * (INW / 128) : KB_ * (DM / 128) + KB_ * (CW / 128) + KB_ * (2 * CW / 128) + (CW / 32) * (DM / 128) + KB_ * (DFF2 / 128) + (DFF / 32) * (DM / 128);
;     const int hi_all = it_hi < NALL ? it_hi : NALL, total = hi_all - it_lo, nwgs = NGW / NWAVES, chunk = (((total + nwgs - 1) / nwgs) + NWAVES - 1) / NWAVES * NWAVES;
;     int it = it_lo + (gw / NWAVES) * chunk + (gw % NWAVES); const int wend0 = it_lo + (gw / NWAVES + 1) * chunk, wend = wend0 < hi_all ? wend0 : hi_all;
; __global__ void __launch_bounds__(NWAVES * 64, 2) mk_fwd(Args args) {
;     ...
;         const int NCONV = (CONV_OVERLAP && G >= 128) ? 51 : 0;
;         if (bx < NCONV) convert_weights<false, true>(P, lds, bx * NWAVES + wave, NCONV * NWAVES, wave, lane, 0, (CONV_OVERLAP && G >= 192) ? LATE_SPLIT : 0x7fffffff);
;         else {
;             sb_phase(lds, PROJ, (bf16*)(ws + WS_MIX), (const float*)(ws + WS_RSB), P.sbo_norm, bx - NCONV, G - NCONV, tid);
;             ret_out_phase(lds, PROJ, (bf16*)(ws + WS_MIX), (const bf16*)(ws + WS_ST), P.ret_norm, bx - NCONV, G - NCONV, tid);
;         }
;         if (NCONV == 0) convert_weights<false>(P, lds, gw, NGW, wave, lane);
.LBB0_519:
	s_mov_b32 s98, 0
	s_and_b32 s99, s2, 1
	s_mov_b32 s100, s80
	s_mov_b32 s101, s56
	v_writelane_b32 v255, s70, 4
	v_writelane_b32 v255, s71, 5
	s_mov_b32 s0, 0x9900
	s_cmp_eq_u32 s80, 0x100
	s_cselect_b32 s1, 1, 0
	s_cmp_gt_i32 s75, 6
	s_cselect_b32 s1, s1, 0
	s_cmp_lg_u32 s1, 0
	s_cselect_b32 s0, 0x6e00, s0
	v_writelane_b32 v255, s0, 2
	s_mov_b32 s0, 0
	v_writelane_b32 v255, s0, 3

; template <bool EARLY> DI bool witem_decode(const Ptrs& P, int it, WItem& d) {
;     ...
;     if (r >= I_OUT + I_Q + I_KV + I_O + I_UP + I_DN) return false;
;     if (r < I_OUT) { const int nb = r % (DM / 128), kb = r / (DM / 128); d = WItem{P.w_out, nullptr, (bf16*)(ws + WS_WOUT), DM, DM, 128 * nb, 128 * nb, 32 * kb, 1}; return true; } r -= I_OUT;
;     if (r < I_Q) { const int nb = r % (CW / 128), kb = r / (CW / 128); d = WItem{P.wq, P.cross_norm, (bf16*)(ws + WS_WQKV), CW, DM, 128 * nb, 128 * nb, 32 * kb, 1}; return true; } r -= I_Q;
;     if (r < I_KV) { const int nb = r % (2 * CW / 128), kb = r / (2 * CW / 128); d = WItem{P.wkv, P.mem_norm, (bf16*)(ws + WS_WQKV), 2 * CW, DM, CW + 128 * nb, 128 * nb, 32 * kb, 1}; return true; } r -= I_KV;
;     if (r < I_O) { const int nb = r % (DM / 128), kb = r / (DM / 128); d = WItem{P.wo, nullptr, (bf16*)(ws + WS_WO), DM, CW, 128 * nb, 128 * nb, 32 * kb, 1}; return true; } r -= I_O;
;     if (r < I_UP) { const int nb = r % (DFF2 / 128), kb = r / (DFF2 / 128), n0 = 128 * nb, src = ((n0 >> 7) & 1) * DFF + 128 * (n0 >> 8);
;         d = WItem{P.w_up, P.ffn_norm, (bf16*)(ws + WS_WUP), DFF2, DM, n0, src, 32 * kb, 1}; return true; } r -= I_UP;
;     { const int nb = r % (DM / 128), kb = r / (DM / 128); d = WItem{P.w_down, nullptr, (bf16*)(ws + WS_WDOWN), DM, DFF, 128 * nb, 128 * nb, 32 * kb, 0}; return true; }
;     ...
;     const int hi_all = it_hi < NALL ? it_hi : NALL, total = hi_all - it_lo, nwgs = NGW / NWAVES, chunk = (((total + nwgs - 1) / nwgs) + NWAVES - 1) / NWAVES * NWAVES;
;     int it = it_lo + (gw / NWAVES) * chunk + (gw % NWAVES); const int wend0 = it_lo + (gw / NWAVES + 1) * chunk, wend = wend0 < hi_all ? wend0 : hi_all;
;     constexpr int ST = NWAVES;
;     bool v0 = it < wend && witem_decode<EARLY>(P, it, d0);
.LBB0_558:
	s_abs_i32 s0, s100
	v_cvt_f32_u32_e32 v2, s0
	s_sub_i32 s4, 0, s0
	v_readlane_b32 s1, v255, 2
	s_nop 3
	s_add_i32 s1, s1, s100
	s_add_i32 s1, s1, -1
	s_xor_b32 s3, s1, s100
	v_rcp_iflag_f32_e32 v2, v2
	s_abs_i32 s1, s1
	s_ashr_i32 s3, s3, 31
	v_mul_f32_e32 v2, 0x4f7ffffe, v2
	v_cvt_u32_f32_e32 v2, v2
	s_nop 0
	v_readfirstlane_b32 s5, v2
	s_mul_i32 s4, s4, s5
	s_mul_hi_u32 s4, s5, s4
	s_add_i32 s5, s5, s4
	s_mul_hi_u32 s4, s1, s5
	s_mul_i32 s5, s4, s0
	s_sub_i32 s1, s1, s5
	s_add_i32 s6, s4, 1
	s_sub_i32 s5, s1, s0
	s_cmp_ge_u32 s1, s0
	s_cselect_b32 s4, s6, s4
	s_cselect_b32 s1, s5, s1
	s_add_i32 s5, s4, 1
	s_cmp_ge_u32 s1, s0
	s_cselect_b32 s0, s5, s4
	s_xor_b32 s0, s0, s3
	s_sub_i32 s0, s0, s3
	s_add_i32 s0, s0, 7
	s_ashr_i32 s1, s101, 31
	s_ashr_i32 s3, s0, 31
	s_lshr_b32 s1, s1, 29
	s_lshr_b32 s3, s3, 29
	s_add_i32 s0, s0, s3
	s_add_i32 s1, s101, s1
	s_and_b32 s0, s0, -8
	s_ashr_i32 s3, s1, 3
	s_and_b32 s1, s1, -8
	s_mul_i32 s3, s0, s3
	s_sub_i32 s1, s101, s1
	s_add_i32 s33, s3, s1
	s_add_i32 s3, s3, s0
	v_readlane_b32 s0, v255, 2
	v_readlane_b32 s1, v255, 3
	s_nop 3
	s_min_i32 s3, s3, s0
	s_add_i32 s3, s3, s1
	s_add_i32 s33, s33, s1
	s_cmp_lg_u32 s99, 0
	s_cselect_b32 s3, s3, 0
	s_cmp_lt_i32 s33, s3
	s_cselect_b64 s[4:5], -1, 0
	s_cmp_ge_i32 s33, s3
	s_cbranch_scc1 .LBB0_565
	s_cmpk_gt_i32 s33, 0xfff
	s_cbranch_scc0 .LBB0_566
	s_cmpk_gt_u32 s33, 0x11ff
	s_cbranch_scc0 .LBB0_567
	s_cmpk_gt_u32 s33, 0x15ff
	s_cbranch_scc0 .LBB0_568
	s_cmpk_gt_u32 s33, 0x17ff
	s_cbranch_scc0 .LBB0_569
	s_cmpk_gt_u32 s33, 0x6dff
	s_cbranch_scc0 .LBB0_570
	s_and_b32 s0, s33, 0x7fffffe0
	s_add_i32 s14, s0, 0xffff9200
	s_add_u32 s12, s84, 0x10800000
	s_addc_u32 s13, s85, 0
	s_lshl_b32 s0, s33, 7
	s_and_b32 s44, s0, 0xf80
	s_mov_b64 s[0:1], 0
	s_mov_b64 s[10:11], 0
	s_mov_b64 s[8:9], s[76:77]
	s_branch .LBB0_571

; #define SEAM(k) do { if (IN(k) && IN((k) + 1)) xcd_barrier(bar); } while (0)
; __device__ __forceinline__ void xcd_barrier(const XcdBarrier& b) {
;     asm volatile("s_waitcnt vmcnt(0)" ::: "memory");
;     __syncthreads();
;     if (threadIdx.x == 0) {
;         unsigned* bar = b.bar;
;         __builtin_amdgcn_s_waitcnt(0);
;         unsigned nloc = b.st[0], nx = b.st[1];
;         if (nloc == 0u) { xcd_barrier_complete(bar, b.x, nloc, nx); b.st[0] = nloc; b.st[1] = nx; }
; __global__ void __launch_bounds__(NWAVES * 64, 2) mk_fwd(Args args) {
;     ...
;         else {
;             sb_phase(lds, PROJ, (bf16*)(ws + WS_MIX), (const float*)(ws + WS_RSB), P.sbo_norm, bx - NCONV, G - NCONV, tid);
;             ret_out_phase(lds, PROJ, (bf16*)(ws + WS_MIX), (const bf16*)(ws + WS_ST), P.ret_norm, bx - NCONV, G - NCONV, tid);
;         }
;         if (NCONV == 0) convert_weights<false>(P, lds, gw, NGW, wave, lane);
;         __syncthreads();
;     }
;     SEAM(4);
.LBB0_727:
	s_waitcnt vmcnt(0) lgkmcnt(0)
	s_barrier
	s_cmp_eq_u32 s98, 2
	s_cbranch_scc1 .Lp6_conv_ret
	s_cmp_eq_u32 s98, 1
	s_cbranch_scc1 .Lp4_done
	s_mov_b32 s98, 1
	s_xor_b32 s99, s99, 1
	v_readlane_b32 s70, v255, 4
	v_readlane_b32 s71, v255, 5
	s_mov_b64 s[4:5], -1
	s_add_u32 s42, s84, 0x26e00000
	s_addc_u32 s43, s85, 0
	s_nop 1
	s_load_dwordx2 s[44:45], s[70:71], 0x20
	s_load_dwordx2 s[50:51], s[70:71], 0x38
	s_waitcnt lgkmcnt(0)
	s_branch .Lp4_conv_entry
.Lp4_done:
.LBB0_728:
	s_cmp_gt_i32 s75, 5
	s_cselect_b64 s[0:1], -1, 0
	s_and_b64 s[4:5], s[70:71], s[0:1]
	s_andn2_b64 vcc, exec, s[4:5]
	s_cbranch_vccnz .LBB0_782
	s_waitcnt vmcnt(0)
	s_waitcnt vmcnt(0)
	s_barrier
	s_mov_b64 s[4:5], exec
	v_readlane_b32 s6, v254, 13
	v_readlane_b32 s7, v254, 14
	s_and_b64 s[6:7], s[4:5], s[6:7]
	s_mov_b64 exec, s[6:7]
	s_cbranch_execz .LBB0_781
	s_add_i32 s3, 0, 0x20160
	v_mov_b32_e32 v2, s3
	s_waitcnt vmcnt(0) expcnt(0) lgkmcnt(0)
	ds_read_b32 v4, v2
	s_add_i32 s3, 0, 0x20164
	v_mov_b32_e32 v2, s3
	ds_read_b32 v2, v2
	s_waitcnt lgkmcnt(1)
	v_cmp_ne_u32_e32 vcc, 0, v4
	s_cbranch_vccnz .LBB0_745
	v_readlane_b32 s6, v254, 0
	v_readlane_b32 s7, v254, 1
	s_load_dwordx2 s[10:11], s[6:7], 0x4
	s_add_u32 s6, s84, 0x4200
	s_addc_u32 s7, s85, 0
	s_add_u32 s8, s84, 0x4400
	s_addc_u32 s9, s85, 0
	s_waitcnt lgkmcnt(0)
	s_mul_i32 s3, s10, s80
	s_add_u32 s10, s84, 0x4500
	s_mul_i32 s3, s3, s11
	s_addc_u32 s11, s85, 0
	s_add_u32 s12, s84, 0x4600
	s_addc_u32 s13, s85, 0
	s_add_u32 s14, s84, 0x4700
	s_addc_u32 s15, s85, 0
	s_add_u32 s16, s84, 0x4800
	s_addc_u32 s17, s85, 0
	s_add_u32 s18, s84, 0x4900
	s_addc_u32 s19, s85, 0
	s_add_u32 s20, s84, 0x4a00
	s_addc_u32 s21, s85, 0
	s_add_u32 s22, s84, 0x4b00
	s_addc_u32 s23, s85, 0
	s_add_u32 s24, s84, 0x4c00
	s_addc_u32 s25, s85, 0
	s_add_u32 s26, s84, 0x4d00
	s_addc_u32 s27, s85, 0
	s_add_u32 s28, s84, 0x4e00
	s_addc_u32 s29, s85, 0
	s_add_u32 s30, s84, 0x4f00
	s_addc_u32 s31, s85, 0
	s_add_u32 s34, s84, 0x5000
	s_addc_u32 s35, s85, 0
	s_add_u32 s36, s84, 0x5100
	s_addc_u32 s37, s85, 0
	s_add_u32 s38, s84, 0x5200
	s_addc_u32 s39, s85, 0
	s_add_u32 s40, s84, 0x5300
	s_addc_u32 s41, s85, 0
	s_mov_b32 s33, 1
	v_mov_b32_e32 v18, 0
	s_branch .LBB0_733

; #define LAS __attribute__((address_space(3)))
; #define LAS __attribute__((address_space(3)))
;     LAS unsigned* scr = (LAS unsigned*)(lds + wave * 16384);
;     WItem d0, d1; WRegs R0, R1;
;     constexpr int KB_ = DM / 32;
;     constexpr int NALL = EARLY ? KB_ * (INW / 128) : KB_ * (DM / 128) + KB_ * (CW / 128) + KB_ * (2 * CW / 128) + (CW / 32) * (DM / 128) + KB_ * (DFF2 / 128) + (DFF / 32) * (DM / 128);
;     const int hi_all = it_hi < NALL ? it_hi : NALL, total = hi_all - it_lo, nwgs = NGW / NWAVES, chunk = (((total + nwgs - 1) / nwgs) + NWAVES - 1) / NWAVES * NWAVES;
;     int it = it_lo + (gw / NWAVES) * chunk + (gw % NWAVES); const int wend0 = it_lo + (gw / NWAVES + 1) * chunk, wend = wend0 < hi_all ? wend0 : hi_all;
; __global__ void __launch_bounds__(NWAVES * 64, 2) mk_fwd(Args args) {
;     ...
;         { pg8::Gemm g{(const bf16*)(ws + WS_MB), (const bf16*)(ws + WS_WQKV) + (size_t)CW * DM, BATCH * NMEM, 2 * CW, DM, DM}; pg8::StaticOrder S; S.init(BATCH * NMEM, 2 * CW, G, (bx + G / 2) % G);
;           pg8::EpiScaleF32 E{(float*)(ws + WS_CKV), 2 * CW, (const float*)(ws + WS_SSQM)};
;           pg8::gemm_phase<pg8::EpiScaleF32, pg8::StaticOrder, true, true>(lds, g, S, E); }
;         if (CONV_OVERLAP && G >= 192 && bx >= G / 2 + 8) { __syncthreads(); convert_weights<false, true>(P, lds, (bx - (G / 2 + 8)) * NWAVES + wave, (G - (G / 2 + 8)) * NWAVES, wave, lane, LATE_SPLIT, 0x7fffffff); }
.LBB0_925:
	s_cmpk_lt_i32 s2, 0x88
	s_cbranch_scc1 .Lp6_hook_done
	s_cmp_lg_u32 s80, 0x100
	s_cbranch_scc1 .Lp6_hook_done
	s_cmp_gt_i32 s74, 4
	s_cbranch_scc1 .Lp6_hook_done
	s_cmp_lt_i32 s75, 7
	s_cbranch_scc1 .Lp6_hook_done
	v_writelane_b32 v255, s8, 8
	v_writelane_b32 v255, s9, 9
	v_writelane_b32 v255, s12, 10
	v_writelane_b32 v255, s16, 11
	v_writelane_b32 v255, s18, 12
	v_writelane_b32 v255, s19, 13
	v_writelane_b32 v255, s20, 14
	v_writelane_b32 v255, s21, 15
	v_writelane_b32 v255, s23, 16
	v_writelane_b32 v255, s24, 17
	v_writelane_b32 v255, s26, 18
	v_writelane_b32 v255, s34, 19
	v_readlane_b32 s70, v254, 0
	v_readlane_b32 s71, v254, 1
	v_and_b32_e32 v1, 63, v0
	v_readfirstlane_b32 s101, v0
	s_sub_u32 s100, s2, 0x88
	s_lshl_b32 s100, s100, 3
	s_sub_u32 s70, s70, 0xc0
	s_subb_u32 s71, s71, 0
	s_lshr_b32 s101, s101, 6
	s_add_u32 s101, s101, s100
	s_mov_b32 s100, 120
	s_mov_b32 s0, 0x2b00
	v_writelane_b32 v255, s0, 2
	s_mov_b32 s0, 0x6e00
	v_writelane_b32 v255, s0, 3
	s_mov_b32 s98, 2
	s_mov_b32 s99, 1
	s_mov_b64 s[4:5], -1
	s_branch .Lp4_conv_entry
